# speedup vs baseline: 1.0737x; 1.0009x over previous
.Lg_top:
	s_cmp_ge_u32 s10, s9
	s_cbranch_scc1 .Lg_noprep0
	v_readlane_b32 s13, v247, s10
	s_add_u32 s14, s12, 0x4b0
	s_add_u32 s15, s12, 0x960
	s_add_u32 s16, s12, 0xe10
	s_nop 1
	s_and_b32 s18, s13, 0xff
	s_cmp_eq_u32 s18, 1
	s_cselect_b32 s42, s12, 0x80000000
	s_and_b32 s18, s13, 0xff00
	s_cmp_eq_u32 s18, 0x100
	s_cselect_b32 s14, s14, 0x80000000
	s_and_b32 s18, s13, 0xff0000
	s_cmp_eq_u32 s18, 0x10000
	s_cselect_b32 s15, s15, 0x80000000
	s_and_b32 s18, s13, 0xff000000
	s_cmp_eq_u32 s18, 0x1000000
	s_cselect_b32 s16, s16, 0x80000000
	v_lshrrev_b32_e64 v249, v240, s13
	v_and_b32_e32 v249, 0xff, v249
	v_cmp_eq_u32_e32 vcc, 1, v249
	s_nop 1
	v_cndmask_b32_e32 v254, v255, v239, vcc
.Lg_noprep0:
	s_sub_u32 s18, s10, 2
	s_cmp_lt_u32 s18, s9
	s_cbranch_scc0 .Lg_s2skip0
	s_cmp_gt_u32 s10, s9
	s_cbranch_scc1 .Lg_s2finalb0
	s_cmp_eq_u32 s10, s9
	s_cbranch_scc1 .Lg_s2final0
	s_waitcnt vmcnt(21)
	v_cvt_pk_f16_f32 v250, v138, v139
	v_cvt_pk_f16_f32 v251, v140, v141
	ds_write_b64 v241, v[250:251] offset:0
	buffer_load_dwordx4 v[138:141], v238, s[20:23], s42 offen nt
	s_waitcnt vmcnt(21)
	v_cvt_pk_f16_f32 v252, v142, v143
	v_cvt_pk_f16_f32 v253, v144, v145
	ds_write_b64 v241, v[252:253] offset:600
	buffer_load_dwordx4 v[142:145], v238, s[24:27], s42 offen nt
	s_waitcnt vmcnt(21)
	v_cvt_pk_f16_f32 v250, v146, v147
	v_cvt_pk_f16_f32 v251, v148, v149
	ds_write_b64 v241, v[250:251] offset:1248
	buffer_load_dwordx4 v[146:149], v238, s[20:23], s14 offen nt
	s_waitcnt vmcnt(21)
	v_cvt_pk_f16_f32 v252, v150, v151
	v_cvt_pk_f16_f32 v253, v152, v153
	ds_write_b64 v241, v[252:253] offset:1848
	buffer_load_dwordx4 v[150:153], v238, s[24:27], s14 offen nt
	s_waitcnt vmcnt(21)
	v_cvt_pk_f16_f32 v250, v154, v155
	v_cvt_pk_f16_f32 v251, v156, v157
	ds_write_b64 v241, v[250:251] offset:2496
	buffer_load_dwordx4 v[154:157], v238, s[20:23], s15 offen nt
	s_waitcnt vmcnt(21)
	v_cvt_pk_f16_f32 v252, v158, v159
	v_cvt_pk_f16_f32 v253, v160, v161
	ds_write_b64 v241, v[252:253] offset:3096
	buffer_load_dwordx4 v[158:161], v238, s[24:27], s15 offen nt
	s_waitcnt vmcnt(21)
	v_cvt_pk_f16_f32 v250, v162, v163
	v_cvt_pk_f16_f32 v251, v164, v165
	ds_write_b64 v241, v[250:251] offset:3744
	buffer_load_dwordx4 v[162:165], v238, s[20:23], s16 offen nt
	s_waitcnt vmcnt(21)
	v_cvt_pk_f16_f32 v252, v166, v167
	v_cvt_pk_f16_f32 v253, v168, v169
	ds_write_b64 v241, v[252:253] offset:4344
	buffer_load_dwordx4 v[166:169], v238, s[24:27], s16 offen nt
	s_mov_b64 exec, s[34:35]
	s_waitcnt vmcnt(21)
	v_cvt_pk_f16_f32 v250, v170, v171
	v_cvt_pk_f16_f32 v251, v172, v173
	ds_write_b64 v242, v[250:251] offset:0
	s_mov_b64 exec, -1
	buffer_load_dwordx4 v[170:173], v254, s[20:23], s12 offen nt
	s_mov_b64 exec, s[34:35]
	s_waitcnt vmcnt(21)
	v_cvt_pk_f16_f32 v252, v174, v175
	v_cvt_pk_f16_f32 v253, v176, v177
	ds_write_b64 v242, v[252:253] offset:600
	s_mov_b64 exec, -1
	buffer_load_dwordx4 v[174:177], v254, s[24:27], s12 offen nt
	s_branch .Lg_s1done0

.Lg_s2finalb0:
	s_waitcnt vmcnt(11)
	v_cvt_pk_f16_f32 v250, v138, v139
	v_cvt_pk_f16_f32 v251, v140, v141
	ds_write_b64 v241, v[250:251] offset:0
	s_waitcnt vmcnt(10)
	v_cvt_pk_f16_f32 v252, v142, v143
	v_cvt_pk_f16_f32 v253, v144, v145
	ds_write_b64 v241, v[252:253] offset:600
	s_waitcnt vmcnt(9)
	v_cvt_pk_f16_f32 v250, v146, v147
	v_cvt_pk_f16_f32 v251, v148, v149
	ds_write_b64 v241, v[250:251] offset:1248
	s_waitcnt vmcnt(8)
	v_cvt_pk_f16_f32 v252, v150, v151
	v_cvt_pk_f16_f32 v253, v152, v153
	ds_write_b64 v241, v[252:253] offset:1848
	s_waitcnt vmcnt(7)
	v_cvt_pk_f16_f32 v250, v154, v155
	v_cvt_pk_f16_f32 v251, v156, v157
	ds_write_b64 v241, v[250:251] offset:2496
	s_waitcnt vmcnt(6)
	v_cvt_pk_f16_f32 v252, v158, v159
	v_cvt_pk_f16_f32 v253, v160, v161
	ds_write_b64 v241, v[252:253] offset:3096
	s_waitcnt vmcnt(5)
	v_cvt_pk_f16_f32 v250, v162, v163
	v_cvt_pk_f16_f32 v251, v164, v165
	ds_write_b64 v241, v[250:251] offset:3744
	s_waitcnt vmcnt(4)
	v_cvt_pk_f16_f32 v252, v166, v167
	v_cvt_pk_f16_f32 v253, v168, v169
	ds_write_b64 v241, v[252:253] offset:4344
	s_mov_b64 exec, s[34:35]
	s_waitcnt vmcnt(3)
	v_cvt_pk_f16_f32 v250, v170, v171
	v_cvt_pk_f16_f32 v251, v172, v173
	ds_write_b64 v242, v[250:251] offset:0
	s_mov_b64 exec, -1
	s_mov_b64 exec, s[34:35]
	s_waitcnt vmcnt(2)
	v_cvt_pk_f16_f32 v252, v174, v175
	v_cvt_pk_f16_f32 v253, v176, v177
	ds_write_b64 v242, v[252:253] offset:600
	s_mov_b64 exec, -1
	s_branch .Lg_s1done0
.Lg_s2skip0:
	s_cmp_ge_u32 s10, s9
	s_cbranch_scc1 .Lg_s1done0
	buffer_load_dwordx4 v[138:141], v238, s[20:23], s42 offen nt
	buffer_load_dwordx4 v[142:145], v238, s[24:27], s42 offen nt
	buffer_load_dwordx4 v[146:149], v238, s[20:23], s14 offen nt
	buffer_load_dwordx4 v[150:153], v238, s[24:27], s14 offen nt
	buffer_load_dwordx4 v[154:157], v238, s[20:23], s15 offen nt
	buffer_load_dwordx4 v[158:161], v238, s[24:27], s15 offen nt
	buffer_load_dwordx4 v[162:165], v238, s[20:23], s16 offen nt
	buffer_load_dwordx4 v[166:169], v238, s[24:27], s16 offen nt
	buffer_load_dwordx4 v[170:173], v254, s[20:23], s12 offen nt
	buffer_load_dwordx4 v[174:177], v254, s[24:27], s12 offen nt

.Lg_noprep1:
	s_sub_u32 s18, s10, 2
	s_cmp_lt_u32 s18, s9
	s_cbranch_scc0 .Lg_s2skip1
	s_cmp_gt_u32 s10, s9
	s_cbranch_scc1 .Lg_s2finalb1
	s_cmp_eq_u32 s10, s9
	s_cbranch_scc1 .Lg_s2final1
	s_waitcnt vmcnt(21)
	v_cvt_pk_f16_f32 v250, v178, v179
	v_cvt_pk_f16_f32 v251, v180, v181
	ds_write_b64 v241, v[250:251] offset:19968
	buffer_load_dwordx4 v[178:181], v238, s[20:23], s42 offen nt
	s_waitcnt vmcnt(21)
	v_cvt_pk_f16_f32 v252, v182, v183
	v_cvt_pk_f16_f32 v253, v184, v185
	ds_write_b64 v241, v[252:253] offset:20568
	buffer_load_dwordx4 v[182:185], v238, s[24:27], s42 offen nt
	s_waitcnt vmcnt(21)
	v_cvt_pk_f16_f32 v250, v186, v187
	v_cvt_pk_f16_f32 v251, v188, v189
	ds_write_b64 v241, v[250:251] offset:21216
	buffer_load_dwordx4 v[186:189], v238, s[20:23], s14 offen nt
	s_waitcnt vmcnt(21)
	v_cvt_pk_f16_f32 v252, v190, v191
	v_cvt_pk_f16_f32 v253, v192, v193
	ds_write_b64 v241, v[252:253] offset:21816
	buffer_load_dwordx4 v[190:193], v238, s[24:27], s14 offen nt
	s_waitcnt vmcnt(21)
	v_cvt_pk_f16_f32 v250, v194, v195
	v_cvt_pk_f16_f32 v251, v196, v197
	ds_write_b64 v241, v[250:251] offset:22464
	buffer_load_dwordx4 v[194:197], v238, s[20:23], s15 offen nt
	s_waitcnt vmcnt(21)
	v_cvt_pk_f16_f32 v252, v198, v199
	v_cvt_pk_f16_f32 v253, v200, v201
	ds_write_b64 v241, v[252:253] offset:23064
	buffer_load_dwordx4 v[198:201], v238, s[24:27], s15 offen nt
	s_waitcnt vmcnt(21)
	v_cvt_pk_f16_f32 v250, v202, v203
	v_cvt_pk_f16_f32 v251, v204, v205
	ds_write_b64 v241, v[250:251] offset:23712
	buffer_load_dwordx4 v[202:205], v238, s[20:23], s16 offen nt
	s_waitcnt vmcnt(21)
	v_cvt_pk_f16_f32 v252, v206, v207
	v_cvt_pk_f16_f32 v253, v208, v209
	ds_write_b64 v241, v[252:253] offset:24312
	buffer_load_dwordx4 v[206:209], v238, s[24:27], s16 offen nt
	s_mov_b64 exec, s[34:35]
	s_waitcnt vmcnt(21)
	v_cvt_pk_f16_f32 v250, v210, v211
	v_cvt_pk_f16_f32 v251, v212, v213
	ds_write_b64 v242, v[250:251] offset:19968
	s_mov_b64 exec, -1
	buffer_load_dwordx4 v[210:213], v254, s[20:23], s12 offen nt
	s_mov_b64 exec, s[34:35]
	s_waitcnt vmcnt(21)
	v_cvt_pk_f16_f32 v252, v214, v215
	v_cvt_pk_f16_f32 v253, v216, v217
	ds_write_b64 v242, v[252:253] offset:20568
	s_mov_b64 exec, -1
	buffer_load_dwordx4 v[214:217], v254, s[24:27], s12 offen nt
	s_branch .Lg_s1done1

.Lg_s2finalb1:
	s_waitcnt vmcnt(11)
	v_cvt_pk_f16_f32 v250, v178, v179
	v_cvt_pk_f16_f32 v251, v180, v181
	ds_write_b64 v241, v[250:251] offset:19968
	s_waitcnt vmcnt(10)
	v_cvt_pk_f16_f32 v252, v182, v183
	v_cvt_pk_f16_f32 v253, v184, v185
	ds_write_b64 v241, v[252:253] offset:20568
	s_waitcnt vmcnt(9)
	v_cvt_pk_f16_f32 v250, v186, v187
	v_cvt_pk_f16_f32 v251, v188, v189
	ds_write_b64 v241, v[250:251] offset:21216
	s_waitcnt vmcnt(8)
	v_cvt_pk_f16_f32 v252, v190, v191
	v_cvt_pk_f16_f32 v253, v192, v193
	ds_write_b64 v241, v[252:253] offset:21816
	s_waitcnt vmcnt(7)
	v_cvt_pk_f16_f32 v250, v194, v195
	v_cvt_pk_f16_f32 v251, v196, v197
	ds_write_b64 v241, v[250:251] offset:22464
	s_waitcnt vmcnt(6)
	v_cvt_pk_f16_f32 v252, v198, v199
	v_cvt_pk_f16_f32 v253, v200, v201
	ds_write_b64 v241, v[252:253] offset:23064
	s_waitcnt vmcnt(5)
	v_cvt_pk_f16_f32 v250, v202, v203
	v_cvt_pk_f16_f32 v251, v204, v205
	ds_write_b64 v241, v[250:251] offset:23712
	s_waitcnt vmcnt(4)
	v_cvt_pk_f16_f32 v252, v206, v207
	v_cvt_pk_f16_f32 v253, v208, v209
	ds_write_b64 v241, v[252:253] offset:24312
	s_mov_b64 exec, s[34:35]
	s_waitcnt vmcnt(3)
	v_cvt_pk_f16_f32 v250, v210, v211
	v_cvt_pk_f16_f32 v251, v212, v213
	ds_write_b64 v242, v[250:251] offset:19968
	s_mov_b64 exec, -1
	s_mov_b64 exec, s[34:35]
	s_waitcnt vmcnt(2)
	v_cvt_pk_f16_f32 v252, v214, v215
	v_cvt_pk_f16_f32 v253, v216, v217
	ds_write_b64 v242, v[252:253] offset:20568
	s_mov_b64 exec, -1
	s_branch .Lg_s1done1
.Lg_s2skip1:
	s_cmp_ge_u32 s10, s9
	s_cbranch_scc1 .Lg_s1done1
	buffer_load_dwordx4 v[178:181], v238, s[20:23], s42 offen nt
	buffer_load_dwordx4 v[182:185], v238, s[24:27], s42 offen nt
	buffer_load_dwordx4 v[186:189], v238, s[20:23], s14 offen nt
	buffer_load_dwordx4 v[190:193], v238, s[24:27], s14 offen nt
	buffer_load_dwordx4 v[194:197], v238, s[20:23], s15 offen nt
	buffer_load_dwordx4 v[198:201], v238, s[24:27], s15 offen nt
	buffer_load_dwordx4 v[202:205], v238, s[20:23], s16 offen nt
	buffer_load_dwordx4 v[206:209], v238, s[24:27], s16 offen nt
	buffer_load_dwordx4 v[210:213], v254, s[20:23], s12 offen nt
	buffer_load_dwordx4 v[214:217], v254, s[24:27], s12 offen nt
